# P2 K-loop: streamer scale+fp8-convert VALU moved out of the load segment into the wave's own MMA4 segment, filling the compiler's s_nop slots between MFMA pairs (branch-free merge with v_bfi)
# speedup vs baseline: 1.0102x; 1.0086x over previous
.LBB0_347:
	v_mov_b32_e32 v152, v204
	v_mov_b32_e32 v153, v234
	v_mov_b32_e32 v154, v235
	v_mov_b32_e32 v155, v236
	ds_read_b128 v[158:161], v217
	ds_read_b128 v[162:165], v218
	ds_read_b128 v[166:169], v219
	ds_read_b128 v[170:173], v220
	ds_read_b128 v[148:151], v221
	ds_read_b128 v[144:147], v222
	ds_read_b128 v[140:143], v223
	ds_read_b128 v[136:139], v224
	ds_read_b128 v[174:177], v233
	ds_read_b128 v[178:181], v233 offset:1024
	ds_read_b128 v[182:185], v233 offset:2048
	ds_read_b128 v[186:189], v233 offset:3072
	ds_read_b128 v[190:193], v233 offset:4096
	ds_read_b128 v[194:197], v233 offset:5120
	ds_read_b128 v[234:237], v233 offset:6144
	ds_read_b128 v[238:241], v233 offset:7168
	s_add_i32 s4, s60, s61
	s_mov_b32 s46, s94
	s_add_i32 s94, s94, 1
	s_add_i32 s5, s4, 0x200
	s_add_i32 s16, s33, s61
	s_cmpk_eq_i32 s61, 0x1e00
	s_cselect_b32 s47, s90, s5
	s_cselect_b32 s97, s91, s16
	s_add_i32 s96, s47, 0x80
	s_mov_b32 m0, s82
	s_add_i32 s5, s4, 0x100180
	buffer_load_dwordx4 v214, s[8:11], s5 offen lds
	s_add_i32 s4, s4, 0x180180
	s_mov_b32 m0, s85
	s_add_i32 vcc_lo, s97, 0x80
	buffer_load_dwordx4 v214, s[8:11], s4 offen lds
	s_lshr_b32 s4, s94, 2
	s_mul_i32 s5, s4, s34
	s_add_i32 s16, s5, s2
	s_cmp_lt_i32 s4, s3
	s_cselect_b64 s[4:5], -1, 0
	s_and_b64 s[44:45], s[4:5], exec
	s_cselect_b32 s16, s16, 0
	s_bfe_u32 s17, s94, 0x10001
	s_or_b32 s17, s17, s83
	s_bfe_u32 s67, s16, 0x50007
	s_bfe_u32 s36, s16, 0x50002
	s_and_b32 s95, s16, 3
	s_cmpk_gt_i32 s16, 0xfff
	s_cselect_b64 s[44:45], -1, 0
	v_lshl_or_b32 v156, s17, 3, v216
	s_and_b64 s[16:17], s[44:45], exec
	s_cselect_b32 s16, s25, s21
	s_cselect_b32 s17, s24, s20
	s_lshl_b32 vcc_hi, s67, 23
	s_add_u32 s17, s17, vcc_hi
	s_addc_u32 s16, s16, 0
	s_lshl_b32 vcc_hi, s36, 18
	s_add_u32 s17, s17, vcc_hi
	s_addc_u32 vcc_hi, s16, 0
	s_lshl_b32 s16, s95, 9
	s_add_u32 s16, s17, s16
	v_and_or_b32 v204, s66, 2, v200
	s_addc_u32 s17, vcc_hi, 0
	v_lshlrev_b64 v[128:129], 11, v[204:205]
	v_lshl_add_u64 v[128:129], s[16:17], 0, v[128:129]
	v_lshlrev_b32_e32 v204, 4, v156
	v_lshl_add_u64 v[132:133], v[128:129], 0, v[204:205]
	global_load_dwordx4 v[128:131], v[132:133], off nt
	s_nop 0
	global_load_dwordx4 v[132:135], v[132:133], off offset:2048 nt
	s_waitcnt vmcnt(10)
	s_waitcnt lgkmcnt(8)
	s_barrier
	s_setprio 1
	s_waitcnt lgkmcnt(7)
	v_mfma_f32_16x16x32_bf16 v[124:127], v[158:161], v[174:177], v[124:127]
	s_waitcnt lgkmcnt(6)
	v_mfma_f32_16x16x32_bf16 v[124:127], v[162:165], v[178:181], v[124:127]
	v_mfma_f32_16x16x32_bf16 v[120:123], v[166:169], v[174:177], v[120:123]
	s_nop 0
	v_mfma_f32_16x16x32_bf16 v[120:123], v[170:173], v[178:181], v[120:123]
	s_waitcnt lgkmcnt(5)
	v_mfma_f32_16x16x32_bf16 v[116:119], v[158:161], v[182:185], v[116:119]
	s_waitcnt lgkmcnt(4)
	v_mfma_f32_16x16x32_bf16 v[116:119], v[162:165], v[186:189], v[116:119]
	v_mfma_f32_16x16x32_bf16 v[112:115], v[166:169], v[182:185], v[112:115]
	s_nop 0
	v_mfma_f32_16x16x32_bf16 v[112:115], v[170:173], v[186:189], v[112:115]
	s_waitcnt lgkmcnt(3)
	v_mfma_f32_16x16x32_bf16 v[108:111], v[158:161], v[190:193], v[108:111]
	s_waitcnt lgkmcnt(2)
	v_mfma_f32_16x16x32_bf16 v[108:111], v[162:165], v[194:197], v[108:111]
	v_mfma_f32_16x16x32_bf16 v[104:107], v[166:169], v[190:193], v[104:107]
	s_nop 0
	v_mfma_f32_16x16x32_bf16 v[104:107], v[170:173], v[194:197], v[104:107]
	s_waitcnt lgkmcnt(1)
	v_mfma_f32_16x16x32_bf16 v[100:103], v[158:161], v[234:237], v[100:103]
	s_waitcnt lgkmcnt(0)
	v_mfma_f32_16x16x32_bf16 v[100:103], v[162:165], v[238:241], v[100:103]
	v_mfma_f32_16x16x32_bf16 v[96:99], v[166:169], v[234:237], v[96:99]
	s_nop 0
	v_mfma_f32_16x16x32_bf16 v[96:99], v[170:173], v[238:241], v[96:99]
	s_setprio 0
	s_setprio 1
	v_mfma_f32_16x16x32_bf16 v[92:95], v[148:151], v[174:177], v[92:95]
	s_nop 0
	v_mfma_f32_16x16x32_bf16 v[92:95], v[144:147], v[178:181], v[92:95]
	v_mfma_f32_16x16x32_bf16 v[88:91], v[140:143], v[174:177], v[88:91]
	s_nop 0
	v_mfma_f32_16x16x32_bf16 v[88:91], v[136:139], v[178:181], v[88:91]
	v_mfma_f32_16x16x32_bf16 v[84:87], v[148:151], v[182:185], v[84:87]
	s_nop 0
	v_mfma_f32_16x16x32_bf16 v[84:87], v[144:147], v[186:189], v[84:87]
	v_mfma_f32_16x16x32_bf16 v[80:83], v[140:143], v[182:185], v[80:83]
	s_nop 0
	v_mfma_f32_16x16x32_bf16 v[80:83], v[136:139], v[186:189], v[80:83]
	v_mfma_f32_16x16x32_bf16 v[76:79], v[148:151], v[190:193], v[76:79]
	s_nop 0
	v_mfma_f32_16x16x32_bf16 v[76:79], v[144:147], v[194:197], v[76:79]
	v_mfma_f32_16x16x32_bf16 v[72:75], v[140:143], v[190:193], v[72:75]
	s_nop 0
	v_mfma_f32_16x16x32_bf16 v[72:75], v[136:139], v[194:197], v[72:75]
	v_mfma_f32_16x16x32_bf16 v[68:71], v[148:151], v[234:237], v[68:71]
	s_nop 0
	v_mfma_f32_16x16x32_bf16 v[68:71], v[144:147], v[238:241], v[68:71]
	v_mfma_f32_16x16x32_bf16 v[64:67], v[140:143], v[234:237], v[64:67]
	s_nop 0
	v_mfma_f32_16x16x32_bf16 v[64:67], v[136:139], v[238:241], v[64:67]
	s_setprio 0
	s_barrier
	ds_read_b128 v[174:177], v233 offset:16384
	ds_read_b128 v[178:181], v233 offset:17408
	ds_read_b128 v[182:185], v233 offset:18432
	ds_read_b128 v[186:189], v233 offset:19456
	ds_read_b128 v[190:193], v233 offset:20480
	ds_read_b128 v[194:197], v233 offset:21504
	ds_read_b128 v[234:237], v233 offset:22528
	ds_read_b128 v[238:241], v233 offset:23552
	s_mov_b32 m0, s65
	s_add_i32 s16, s97, 0x100000
	buffer_load_dwordx4 v215, s[12:15], s97 offen lds
	s_mov_b32 m0, s68
	s_nop 0
	buffer_load_dwordx4 v215, s[12:15], s16 offen lds
	s_add_i32 s16, s97, 0x10000
	s_mov_b32 m0, s69
	s_nop 0
	buffer_load_dwordx4 v215, s[12:15], s16 offen lds
	s_add_i32 s16, s97, 0x110000
	s_mov_b32 m0, s70
	s_nop 0
	buffer_load_dwordx4 v215, s[12:15], s16 offen lds
	s_mov_b32 m0, s64
	s_add_i32 s16, s47, 0x80000
	buffer_load_dwordx4 v214, s[8:11], s47 offen lds
	s_mov_b32 m0, s71
	s_nop 0
	buffer_load_dwordx4 v214, s[8:11], s16 offen lds
	s_waitcnt vmcnt(10)
	s_waitcnt lgkmcnt(6)
	s_barrier
	s_setprio 1
	s_waitcnt lgkmcnt(7)
	v_mfma_f32_16x16x32_bf16 v[60:63], v[158:161], v[174:177], v[60:63]
	s_waitcnt lgkmcnt(6)
	v_mfma_f32_16x16x32_bf16 v[60:63], v[162:165], v[178:181], v[60:63]
	v_mfma_f32_16x16x32_bf16 v[56:59], v[166:169], v[174:177], v[56:59]
	s_nop 0
	v_mfma_f32_16x16x32_bf16 v[56:59], v[170:173], v[178:181], v[56:59]
	s_waitcnt lgkmcnt(5)
	v_mfma_f32_16x16x32_bf16 v[52:55], v[158:161], v[182:185], v[52:55]
	s_waitcnt lgkmcnt(4)
	v_mfma_f32_16x16x32_bf16 v[52:55], v[162:165], v[186:189], v[52:55]
	v_mfma_f32_16x16x32_bf16 v[48:51], v[166:169], v[182:185], v[48:51]
	s_nop 0
	v_mfma_f32_16x16x32_bf16 v[48:51], v[170:173], v[186:189], v[48:51]
	s_waitcnt lgkmcnt(3)
	v_mfma_f32_16x16x32_bf16 v[44:47], v[158:161], v[190:193], v[44:47]
	s_waitcnt lgkmcnt(2)
	v_mfma_f32_16x16x32_bf16 v[44:47], v[162:165], v[194:197], v[44:47]
	v_mfma_f32_16x16x32_bf16 v[40:43], v[166:169], v[190:193], v[40:43]
	s_nop 0
	v_mfma_f32_16x16x32_bf16 v[40:43], v[170:173], v[194:197], v[40:43]
	s_waitcnt lgkmcnt(1)
	v_mfma_f32_16x16x32_bf16 v[36:39], v[158:161], v[234:237], v[36:39]
	s_waitcnt lgkmcnt(0)
	v_mfma_f32_16x16x32_bf16 v[36:39], v[162:165], v[238:241], v[36:39]
	v_mfma_f32_16x16x32_bf16 v[32:35], v[166:169], v[234:237], v[32:35]
	s_nop 0
	v_mfma_f32_16x16x32_bf16 v[32:35], v[170:173], v[238:241], v[32:35]
	s_setprio 0
	s_setprio 1
	v_mfma_f32_16x16x32_bf16 v[28:31], v[148:151], v[174:177], v[28:31]
	s_nop 0
	v_mfma_f32_16x16x32_bf16 v[28:31], v[144:147], v[178:181], v[28:31]
	v_mfma_f32_16x16x32_bf16 v[24:27], v[140:143], v[174:177], v[24:27]
	s_nop 0
	v_mfma_f32_16x16x32_bf16 v[24:27], v[136:139], v[178:181], v[24:27]
	v_mfma_f32_16x16x32_bf16 v[20:23], v[148:151], v[182:185], v[20:23]
	s_nop 0
	v_mfma_f32_16x16x32_bf16 v[20:23], v[144:147], v[186:189], v[20:23]
	v_mfma_f32_16x16x32_bf16 v[16:19], v[140:143], v[182:185], v[16:19]
	s_nop 0
	v_mfma_f32_16x16x32_bf16 v[16:19], v[136:139], v[186:189], v[16:19]
	v_mfma_f32_16x16x32_bf16 v[12:15], v[148:151], v[190:193], v[12:15]
	s_nop 0
	v_mfma_f32_16x16x32_bf16 v[12:15], v[144:147], v[194:197], v[12:15]
	v_mfma_f32_16x16x32_bf16 v[8:11], v[140:143], v[190:193], v[8:11]
	s_nop 0
	v_mfma_f32_16x16x32_bf16 v[8:11], v[136:139], v[194:197], v[8:11]
	v_mfma_f32_16x16x32_bf16 v[4:7], v[148:151], v[234:237], v[4:7]
	s_nop 0
	v_mfma_f32_16x16x32_bf16 v[4:7], v[144:147], v[238:241], v[4:7]
	v_mfma_f32_16x16x32_bf16 v[0:3], v[140:143], v[234:237], v[0:3]
	s_nop 0
	v_mfma_f32_16x16x32_bf16 v[0:3], v[136:139], v[238:241], v[0:3]
	s_setprio 0
	s_barrier
	ds_read_b128 v[136:139], v225
	ds_read_b128 v[140:143], v226
	ds_read_b128 v[144:147], v227
	ds_read_b128 v[148:151], v228
	ds_read_b128 v[158:161], v229
	ds_read_b128 v[162:165], v230
	ds_read_b128 v[166:169], v231
	ds_read_b128 v[170:173], v232
	ds_read_b128 v[174:177], v233 offset:32768
	ds_read_b128 v[178:181], v233 offset:33792
	ds_read_b128 v[182:185], v233 offset:34816
	ds_read_b128 v[186:189], v233 offset:35840
	ds_read_b128 v[190:193], v233 offset:36864
	ds_read_b128 v[194:197], v233 offset:37888
	ds_read_b128 v[234:237], v233 offset:38912
	ds_read_b128 v[238:241], v233 offset:39936
	s_mov_b32 m0, s72
	s_add_i32 s16, s47, 0x100000
	buffer_load_dwordx4 v214, s[8:11], s16 offen lds
	s_add_i32 s16, s47, 0x180000
	s_mov_b32 m0, s73
	s_nop 0
	buffer_load_dwordx4 v214, s[8:11], s16 offen lds
	s_waitcnt vmcnt(10)
	s_waitcnt lgkmcnt(8)
	s_barrier
	s_setprio 1
	s_waitcnt lgkmcnt(7)
	v_mfma_f32_16x16x32_bf16 v[124:127], v[136:139], v[174:177], v[124:127]
	s_waitcnt lgkmcnt(6)
	v_mfma_f32_16x16x32_bf16 v[124:127], v[140:143], v[178:181], v[124:127]
	v_mfma_f32_16x16x32_bf16 v[120:123], v[144:147], v[174:177], v[120:123]
	s_nop 0
	v_mfma_f32_16x16x32_bf16 v[120:123], v[148:151], v[178:181], v[120:123]
	s_waitcnt lgkmcnt(5)
	v_mfma_f32_16x16x32_bf16 v[116:119], v[136:139], v[182:185], v[116:119]
	s_waitcnt lgkmcnt(4)
	v_mfma_f32_16x16x32_bf16 v[116:119], v[140:143], v[186:189], v[116:119]
	v_mfma_f32_16x16x32_bf16 v[112:115], v[144:147], v[182:185], v[112:115]
	s_nop 0
	v_mfma_f32_16x16x32_bf16 v[112:115], v[148:151], v[186:189], v[112:115]
	s_waitcnt lgkmcnt(3)
	v_mfma_f32_16x16x32_bf16 v[108:111], v[136:139], v[190:193], v[108:111]
	s_waitcnt lgkmcnt(2)
	v_mfma_f32_16x16x32_bf16 v[108:111], v[140:143], v[194:197], v[108:111]
	v_mfma_f32_16x16x32_bf16 v[104:107], v[144:147], v[190:193], v[104:107]
	s_nop 0
	v_mfma_f32_16x16x32_bf16 v[104:107], v[148:151], v[194:197], v[104:107]
	s_waitcnt lgkmcnt(1)
	v_mfma_f32_16x16x32_bf16 v[100:103], v[136:139], v[234:237], v[100:103]
	s_waitcnt lgkmcnt(0)
	v_mfma_f32_16x16x32_bf16 v[100:103], v[140:143], v[238:241], v[100:103]
	v_mfma_f32_16x16x32_bf16 v[96:99], v[144:147], v[234:237], v[96:99]
	s_nop 0
	v_mfma_f32_16x16x32_bf16 v[96:99], v[148:151], v[238:241], v[96:99]
	s_setprio 0
	s_setprio 1
	v_mfma_f32_16x16x32_bf16 v[92:95], v[158:161], v[174:177], v[92:95]
	s_nop 0
	v_mfma_f32_16x16x32_bf16 v[92:95], v[162:165], v[178:181], v[92:95]
	v_mfma_f32_16x16x32_bf16 v[88:91], v[166:169], v[174:177], v[88:91]
	s_nop 0
	v_mfma_f32_16x16x32_bf16 v[88:91], v[170:173], v[178:181], v[88:91]
	v_mfma_f32_16x16x32_bf16 v[84:87], v[158:161], v[182:185], v[84:87]
	s_nop 0
	v_mfma_f32_16x16x32_bf16 v[84:87], v[162:165], v[186:189], v[84:87]
	v_mfma_f32_16x16x32_bf16 v[80:83], v[166:169], v[182:185], v[80:83]
	s_nop 0
	v_mfma_f32_16x16x32_bf16 v[80:83], v[170:173], v[186:189], v[80:83]
	v_mfma_f32_16x16x32_bf16 v[76:79], v[158:161], v[190:193], v[76:79]
	s_nop 0
	v_mfma_f32_16x16x32_bf16 v[76:79], v[162:165], v[194:197], v[76:79]
	v_mfma_f32_16x16x32_bf16 v[72:75], v[166:169], v[190:193], v[72:75]
	s_nop 0
	v_mfma_f32_16x16x32_bf16 v[72:75], v[170:173], v[194:197], v[72:75]
	v_mfma_f32_16x16x32_bf16 v[68:71], v[158:161], v[234:237], v[68:71]
	s_nop 0
	v_mfma_f32_16x16x32_bf16 v[68:71], v[162:165], v[238:241], v[68:71]
	v_mfma_f32_16x16x32_bf16 v[64:67], v[166:169], v[234:237], v[64:67]
	s_nop 0
	v_mfma_f32_16x16x32_bf16 v[64:67], v[170:173], v[238:241], v[64:67]
	s_setprio 0
	s_barrier
	ds_read_b128 v[174:177], v233 offset:49152
	ds_read_b128 v[178:181], v233 offset:50176
	ds_read_b128 v[182:185], v233 offset:51200
	ds_read_b128 v[186:189], v233 offset:52224
	ds_read_b128 v[190:193], v233 offset:53248
	ds_read_b128 v[194:197], v233 offset:54272
	ds_read_b128 v[234:237], v233 offset:55296
	ds_read_b128 v[238:241], v233 offset:56320
	s_mov_b32 m0, s76
	s_add_i32 s16, s97, 0x100080
	buffer_load_dwordx4 v215, s[12:15], vcc_lo offen lds
	s_mov_b32 m0, s77
	s_add_i32 s47, s47, 0x80080
	buffer_load_dwordx4 v215, s[12:15], s16 offen lds
	s_add_i32 s16, s97, 0x10080
	s_mov_b32 m0, s80
	s_add_i32 s97, s97, 0x110080
	buffer_load_dwordx4 v215, s[12:15], s16 offen lds
	s_mov_b32 m0, s81
	s_nop 0
	buffer_load_dwordx4 v215, s[12:15], s97 offen lds
	s_mov_b32 m0, s78
	s_nop 0
	buffer_load_dwordx4 v214, s[8:11], s96 offen lds
	s_mov_b32 m0, s79
	s_nop 0
	buffer_load_dwordx4 v214, s[8:11], s47 offen lds
	s_bitcmp0_b32 s46, 0
	s_mov_b32 s98, 0xffff
	s_cselect_b32 s98, 0xffff0000, s98
	s_waitcnt vmcnt(8)
	s_waitcnt lgkmcnt(6)
	s_barrier
	s_setprio 1
	s_waitcnt lgkmcnt(7)
	v_mfma_f32_16x16x32_bf16 v[60:63], v[136:139], v[174:177], v[60:63]
	s_waitcnt lgkmcnt(6)
	v_mfma_f32_16x16x32_bf16 v[60:63], v[140:143], v[178:181], v[60:63]
	v_mfma_f32_16x16x32_bf16 v[56:59], v[144:147], v[174:177], v[56:59]
	v_mul_f32_e32 v128, 0x42800000, v128
	v_mfma_f32_16x16x32_bf16 v[56:59], v[148:151], v[178:181], v[56:59]
	v_mul_f32_e32 v130, 0x42800000, v130
	s_waitcnt lgkmcnt(5)
	v_mfma_f32_16x16x32_bf16 v[52:55], v[136:139], v[182:185], v[52:55]
	s_waitcnt lgkmcnt(4)
	v_mfma_f32_16x16x32_bf16 v[52:55], v[140:143], v[186:189], v[52:55]
	v_mfma_f32_16x16x32_bf16 v[48:51], v[144:147], v[182:185], v[48:51]
	v_mul_f32_e32 v132, 0x42800000, v132
	v_mfma_f32_16x16x32_bf16 v[48:51], v[148:151], v[186:189], v[48:51]
	v_mul_f32_e32 v134, 0x42800000, v134
	s_waitcnt lgkmcnt(3)
	v_mfma_f32_16x16x32_bf16 v[44:47], v[136:139], v[190:193], v[44:47]
	s_waitcnt lgkmcnt(2)
	v_mfma_f32_16x16x32_bf16 v[44:47], v[140:143], v[194:197], v[44:47]
	v_mfma_f32_16x16x32_bf16 v[40:43], v[144:147], v[190:193], v[40:43]
	v_mul_f32_e32 v129, 0x42800000, v129
	v_mfma_f32_16x16x32_bf16 v[40:43], v[148:151], v[194:197], v[40:43]
	v_mul_f32_e32 v131, 0x42800000, v131
	s_waitcnt lgkmcnt(1)
	v_mfma_f32_16x16x32_bf16 v[36:39], v[136:139], v[234:237], v[36:39]
	s_waitcnt lgkmcnt(0)
	v_mfma_f32_16x16x32_bf16 v[36:39], v[140:143], v[238:241], v[36:39]
	v_mfma_f32_16x16x32_bf16 v[32:35], v[144:147], v[234:237], v[32:35]
	v_mul_f32_e32 v133, 0x42800000, v133
	v_mfma_f32_16x16x32_bf16 v[32:35], v[148:151], v[238:241], v[32:35]
	v_mul_f32_e32 v135, 0x42800000, v135
	s_setprio 0
	s_setprio 1
	v_mfma_f32_16x16x32_bf16 v[28:31], v[158:161], v[174:177], v[28:31]
	v_cvt_pk_fp8_f32 v204, v128, v132
	v_mfma_f32_16x16x32_bf16 v[28:31], v[162:165], v[178:181], v[28:31]
	v_mfma_f32_16x16x32_bf16 v[24:27], v[166:169], v[174:177], v[24:27]
	v_cvt_pk_fp8_f32 v204, v128, v132 op_sel:[0,0,1]
	v_mfma_f32_16x16x32_bf16 v[24:27], v[170:173], v[178:181], v[24:27]
	v_mfma_f32_16x16x32_bf16 v[20:23], v[158:161], v[182:185], v[20:23]
	v_cvt_pk_fp8_f32 v250, v129, v133
	v_mfma_f32_16x16x32_bf16 v[20:23], v[162:165], v[186:189], v[20:23]
	v_mfma_f32_16x16x32_bf16 v[16:19], v[166:169], v[182:185], v[16:19]
	v_cvt_pk_fp8_f32 v250, v129, v133 op_sel:[0,0,1]
	v_mfma_f32_16x16x32_bf16 v[16:19], v[170:173], v[186:189], v[16:19]
	v_mfma_f32_16x16x32_bf16 v[12:15], v[158:161], v[190:193], v[12:15]
	v_cvt_pk_fp8_f32 v251, v130, v134
	v_mfma_f32_16x16x32_bf16 v[12:15], v[162:165], v[194:197], v[12:15]
	v_bfi_b32 v152, s98, v204, v152
	v_mfma_f32_16x16x32_bf16 v[8:11], v[166:169], v[190:193], v[8:11]
	v_cvt_pk_fp8_f32 v251, v130, v134 op_sel:[0,0,1]
	v_mfma_f32_16x16x32_bf16 v[8:11], v[170:173], v[194:197], v[8:11]
	v_bfi_b32 v153, s98, v250, v153
	v_mfma_f32_16x16x32_bf16 v[4:7], v[158:161], v[234:237], v[4:7]
	v_cvt_pk_fp8_f32 v252, v131, v135
	v_mfma_f32_16x16x32_bf16 v[4:7], v[162:165], v[238:241], v[4:7]
	v_bfi_b32 v154, s98, v251, v154
	v_mfma_f32_16x16x32_bf16 v[0:3], v[166:169], v[234:237], v[0:3]
	v_cvt_pk_fp8_f32 v252, v131, v135 op_sel:[0,0,1]
	v_mfma_f32_16x16x32_bf16 v[0:3], v[170:173], v[238:241], v[0:3]
	v_bfi_b32 v155, s98, v252, v155
	s_setprio 0
	s_barrier
	s_bitcmp0_b32 s46, 0
	s_mov_b64 s[46:47], -1
	s_cbranch_scc0 .LBB0_345
	s_andn2_b64 vcc, exec, s[4:5]
	s_cbranch_vccnz .LBB0_345
	s_lshl_b32 s4, s67, 10
	s_lshl_b32 s5, s95, 8
	s_or_b32 s16, s4, s5
	s_and_b64 s[4:5], s[44:45], exec
	s_cselect_b32 s4, 8, 0
	v_lshlrev_b32_e32 v128, 3, v156
	s_or_b32 s4, s4, s16
	v_and_b32_e32 v128, 0xf0, v128
	v_or_b32_e32 v128, s4, v128
	v_or_b32_e32 v204, v128, v202
	v_lshlrev_b64 v[128:129], 12, v[204:205]
	v_lshl_add_u64 v[128:129], s[6:7], 0, v[128:129]
	s_lshl_b32 s36, s36, 7
	v_lshl_add_u64 v[128:129], v[128:129], 0, s[36:37]
	v_lshl_add_u64 v[128:129], v[128:129], 0, v[200:201]
	v_add_co_u32_e32 v130, vcc, 0x1000, v128
	global_store_dword v[128:129], v152, off
	s_nop 0
	v_addc_co_u32_e32 v131, vcc, 0, v129, vcc
	global_store_dword v[130:131], v153, off
	v_add_co_u32_e32 v130, vcc, 0x2000, v128
	s_nop 1
	v_addc_co_u32_e32 v131, vcc, 0, v129, vcc
	v_add_co_u32_e32 v128, vcc, 0x3000, v128
	global_store_dword v[130:131], v154, off
	s_nop 0
	v_addc_co_u32_e32 v129, vcc, 0, v129, vcc
	global_store_dword v[128:129], v155, off
	s_branch .LBB0_345
